# combo_1
# speedup vs baseline: 1.0349x; 1.0349x over previous
_Z10gae_kernelPKfPKiS2_S0_S0_S0_PfS3_:
	s_load_dwordx8 s[4:11], s[0:1], 0x0
	s_load_dwordx4 s[12:15], s[0:1], 0x20
	v_and_b32_e32 v64, 63, v0
	v_lshrrev_b32_e32 v1, 6, v0
	s_andn2_b32 s16, s2, 63
	s_and_b32 s17, s2, 7
	s_lshl_b32 s17, s17, 3
	s_bfe_u32 s18, s2, 0x30003
	s_or_b32 s16, s16, s17
	s_or_b32 s2, s16, s18
	s_mov_b32 s3, 0
	s_lshl_b64 s[2:3], s[2:3], 11
	v_lshlrev_b32_e32 v2, 9, v1
	v_lshlrev_b32_e32 v3, 2, v64
	v_or3_b32 v2, s2, v2, v3
	v_mov_b32_e32 v3, s3
	v_lshlrev_b64 v[18:19], 2, v[2:3]
	s_waitcnt lgkmcnt(0)
	v_lshl_add_u64 v[54:55], s[14:15], 0, v[18:19]
	v_lshl_add_u64 v[52:53], s[6:7], 0, v[18:19]
	global_load_dwordx4 v[10:13], v[54:55], off sc0 sc1 nt
	global_load_dwordx4 v[14:17], v[52:53], off sc0 sc1 nt
	v_lshl_add_u64 v[56:57], s[8:9], 0, v[18:19]
	global_load_dwordx4 v[20:23], v[56:57], off sc0 sc1 nt
	v_lshl_add_u64 v[58:59], s[12:13], 0, v[18:19]
	global_load_dwordx4 v[24:27], v[58:59], off sc0 sc1 nt
	v_lshl_add_u64 v[60:61], s[4:5], 0, v[18:19]
	global_load_dwordx4 v[28:31], v[60:61], off sc0 sc1 nt
	v_lshl_add_u64 v[62:63], s[10:11], 0, v[18:19]
	global_load_dwordx4 v[2:5], v[62:63], off sc0 sc1 nt
	global_load_dwordx4 v[32:35], v[60:61], off offset:1024 sc0 sc1 nt
	global_load_dwordx4 v[36:39], v[52:53], off offset:1024 sc0 sc1 nt
	global_load_dwordx4 v[40:43], v[56:57], off offset:1024 sc0 sc1 nt
	global_load_dwordx4 v[6:9], v[62:63], off offset:1024 sc0 sc1 nt
	global_load_dwordx4 v[44:47], v[58:59], off offset:1024 sc0 sc1 nt
	global_load_dwordx4 v[48:51], v[54:55], off offset:1024 sc0 sc1 nt
	v_mov_b32_e32 v66, 0
	v_mov_b32_e32 v68, 1.0
	v_mov_b32_e32 v69, 0
	v_mov_b32_e32 v70, 1.0
	v_mov_b32_e32 v71, 0
	v_mov_b32_e32 v72, 1.0
	v_bfe_u32 v73, v0, 4, 2
	v_cmp_gt_u32_e64 s[4:5], 16, v64
	v_mov_b32_e32 v65, 0
	v_mov_b32_e32 v67, 1.0
	s_waitcnt vmcnt(11)
	v_mul_f32_e32 v12, 0x3f7d70a4, v12
	s_waitcnt vmcnt(10)
	v_cmp_eq_u32_e32 vcc, 0, v14
	v_mul_f32_e32 v13, 0x3f7d70a4, v13
	v_mul_f32_e32 v10, 0x3f7d70a4, v10
	v_cndmask_b32_e64 v14, 0, 1.0, vcc
	s_waitcnt vmcnt(9)
	v_cmp_eq_u32_e32 vcc, 0, v20
	v_mul_f32_e32 v11, 0x3f7d70a4, v11
	s_waitcnt vmcnt(8)
	v_mul_f32_e32 v26, v26, v12
	v_cndmask_b32_e64 v20, 0, 1.0, vcc
	v_cmp_eq_u32_e32 vcc, 0, v15
	v_mul_f32_e32 v27, v27, v13
	v_mul_f32_e32 v24, v24, v10
	v_cndmask_b32_e64 v15, 0, 1.0, vcc
	v_cmp_eq_u32_e32 vcc, 0, v21
	v_mul_f32_e32 v25, v25, v11
	v_mul_f32_e32 v12, 0x3f733333, v12
	v_cndmask_b32_e64 v21, 0, 1.0, vcc
	v_cmp_eq_u32_e32 vcc, 0, v16
	v_mul_f32_e32 v13, 0x3f733333, v13
	v_mul_f32_e32 v10, 0x3f733333, v10
	v_cndmask_b32_e64 v16, 0, 1.0, vcc
	v_cmp_eq_u32_e32 vcc, 0, v22
	s_waitcnt vmcnt(7)
	v_fma_f32 v16, v26, v16, v30
	v_mul_f32_e32 v11, 0x3f733333, v11
	v_cndmask_b32_e64 v22, 0, 1.0, vcc
	v_cmp_eq_u32_e32 vcc, 0, v17
	v_fma_f32 v14, v24, v14, v28
	v_fma_f32 v15, v25, v15, v29
	v_cndmask_b32_e64 v17, 0, 1.0, vcc
	v_cmp_eq_u32_e32 vcc, 0, v23
	v_fmac_f32_e32 v31, v27, v17
	v_mul_f32_e32 v22, v12, v22
	v_cndmask_b32_e64 v23, 0, 1.0, vcc
	v_mul_f32_e32 v23, v13, v23
	s_waitcnt vmcnt(6)
	v_sub_f32_e32 v12, v16, v4
	v_sub_f32_e32 v13, v31, v5
	v_mul_f32_e32 v20, v10, v20
	v_mul_f32_e32 v21, v11, v21
	v_sub_f32_e32 v10, v14, v2
	v_sub_f32_e32 v11, v15, v3
	v_mul_f32_e32 v14, v23, v22
	v_fma_f32 v15, v22, v13, v12
	v_mul_f32_e32 v14, v14, v21
	v_fma_f32 v15, v21, v15, v11
	v_mul_f32_e32 v14, v14, v20
	v_fma_f32 v24, v20, v15, v10
	v_mov_b32_e32 v16, 1.0
	v_mov_b32_dpp v68, v14 row_shl:1 row_mask:0xf bank_mask:0xf
	v_mov_b32_dpp v66, v24 row_shl:1 row_mask:0xf bank_mask:0xf
	v_mul_f32_e32 v15, v14, v68
	v_fmac_f32_e32 v24, v14, v66
	v_cmp_eq_u32_e32 vcc, 2, v73
	v_mov_b32_dpp v70, v15 row_shl:2 row_mask:0xf bank_mask:0xf
	v_mov_b32_dpp v69, v24 row_shl:2 row_mask:0xf bank_mask:0xf
	v_mul_f32_e32 v14, v15, v70
	v_fmac_f32_e32 v24, v15, v69
	v_mov_b32_e32 v15, 0
	v_mov_b32_dpp v72, v14 row_shl:4 row_mask:0xf bank_mask:0xf
	v_mov_b32_dpp v71, v24 row_shl:4 row_mask:0xf bank_mask:0xf
	v_fmac_f32_e32 v24, v14, v71
	v_mul_f32_e32 v14, v14, v72
	s_nop 0
	v_mov_b32_dpp v15, v24 row_shl:8 row_mask:0xf bank_mask:0xf
	v_mov_b32_dpp v16, v14 row_shl:8 row_mask:0xf bank_mask:0xf
	v_fmac_f32_e32 v24, v14, v15
	v_mul_f32_e32 v14, v14, v16
	v_readlane_b32 s9, v24, 32
	v_readlane_b32 s2, v14, 48
	v_readlane_b32 s8, v14, 32
	v_readlane_b32 s6, v14, 16
	v_mov_b32_e32 v15, s2
	v_mul_f32_e32 v16, s8, v15
	v_cndmask_b32_e32 v15, 1.0, v15, vcc
	v_cmp_eq_u32_e64 s[2:3], 1, v73
	v_readlane_b32 s10, v24, 48
	v_mul_f32_e32 v17, s6, v16
	v_cndmask_b32_e64 v15, v15, v16, s[2:3]
	v_readlane_b32 s7, v24, 16
	v_cndmask_b32_e64 v15, v15, v17, s[4:5]
	v_mov_b32_e32 v16, s9
	v_mov_b32_e32 v17, s10
	v_fmac_f32_e32 v16, s8, v17
	v_mov_b32_e32 v25, s7
	v_cndmask_b32_e32 v17, 0, v17, vcc
	v_fmac_f32_e32 v25, s6, v16
	v_cndmask_b32_e64 v16, v17, v16, s[2:3]
	v_cndmask_b32_e64 v16, v16, v25, s[4:5]
	s_waitcnt vmcnt(4)
	v_cmp_eq_u32_e64 s[6:7], 0, v36
	v_fmac_f32_e32 v24, v14, v16
	v_mul_f32_e32 v28, v14, v15
	s_waitcnt vmcnt(0)
	v_mul_f32_e32 v15, 0x3f7d70a4, v48
	v_cndmask_b32_e64 v14, 0, 1.0, s[6:7]
	v_cmp_eq_u32_e64 s[6:7], 0, v40
	v_mul_f32_e32 v17, v44, v15
	v_mul_f32_e32 v15, 0x3f733333, v15
	v_cndmask_b32_e64 v16, 0, 1.0, s[6:7]
	v_cmp_eq_u32_e64 s[6:7], 0, v37
	v_mul_f32_e32 v25, v15, v16
	v_mul_f32_e32 v16, 0x3f7d70a4, v49
	v_cndmask_b32_e64 v15, 0, 1.0, s[6:7]
	v_cmp_eq_u32_e64 s[6:7], 0, v41
	v_fma_f32 v14, v17, v14, v32
	v_mul_f32_e32 v26, v45, v16
	v_cndmask_b32_e64 v17, 0, 1.0, s[6:7]
	v_mul_f32_e32 v16, 0x3f733333, v16
	v_fma_f32 v15, v26, v15, v33
	v_mul_f32_e32 v26, v16, v17
	v_mul_f32_e32 v17, 0x3f7d70a4, v50
	v_cmp_eq_u32_e64 s[6:7], 0, v38
	v_mul_f32_e32 v29, v46, v17
	v_mul_f32_e32 v17, 0x3f733333, v17
	v_cndmask_b32_e64 v16, 0, 1.0, s[6:7]
	v_cmp_eq_u32_e64 s[6:7], 0, v42
	v_fma_f32 v16, v29, v16, v34
	v_mul_f32_e32 v29, 0x3f7d70a4, v51
	v_cndmask_b32_e64 v27, 0, 1.0, s[6:7]
	v_cmp_eq_u32_e64 s[6:7], 0, v39
	v_mul_f32_e32 v27, v17, v27
	v_mul_f32_e32 v31, v47, v29
	v_cndmask_b32_e64 v17, 0, 1.0, s[6:7]
	v_cmp_eq_u32_e64 s[6:7], 0, v43
	v_fmac_f32_e32 v35, v31, v17
	v_mul_f32_e32 v29, 0x3f733333, v29
	v_cndmask_b32_e64 v30, 0, 1.0, s[6:7]
	v_sub_f32_e32 v16, v16, v8
	v_sub_f32_e32 v17, v35, v9
	v_mul_f32_e32 v29, v29, v30
	v_sub_f32_e32 v15, v15, v7
	v_fma_f32 v30, v27, v17, v16
	v_mul_f32_e32 v31, v29, v27
	v_sub_f32_e32 v14, v14, v6
	v_fma_f32 v30, v26, v30, v15
	v_mul_f32_e32 v31, v31, v26
	v_fma_f32 v30, v25, v30, v14
	v_mul_f32_e32 v31, v31, v25
	v_mov_b32_e32 v32, 0
	v_mov_b32_e32 v33, 1.0
	s_nop 0
	v_mov_b32_dpp v32, v30 row_shl:1 row_mask:0xf bank_mask:0xf
	v_mov_b32_dpp v33, v31 row_shl:1 row_mask:0xf bank_mask:0xf
	v_fmac_f32_e32 v30, v31, v32
	v_mul_f32_e32 v31, v31, v33
	v_mov_b32_e32 v32, 0
	v_mov_b32_e32 v33, 1.0
	s_nop 0
	v_mov_b32_dpp v32, v30 row_shl:2 row_mask:0xf bank_mask:0xf
	v_mov_b32_dpp v33, v31 row_shl:2 row_mask:0xf bank_mask:0xf
	v_fmac_f32_e32 v30, v31, v32
	v_mul_f32_e32 v31, v31, v33
	v_mov_b32_e32 v32, 0
	v_mov_b32_e32 v33, 1.0
	s_nop 0
	v_mov_b32_dpp v32, v30 row_shl:4 row_mask:0xf bank_mask:0xf
	v_mov_b32_dpp v33, v31 row_shl:4 row_mask:0xf bank_mask:0xf
	v_fmac_f32_e32 v30, v31, v32
	v_mul_f32_e32 v31, v31, v33
	s_nop 0
	v_mov_b32_dpp v65, v30 row_shl:8 row_mask:0xf bank_mask:0xf
	v_mov_b32_dpp v67, v31 row_shl:8 row_mask:0xf bank_mask:0xf
	v_fmac_f32_e32 v30, v31, v65
	v_mul_f32_e32 v31, v31, v67
	v_readlane_b32 s9, v30, 32
	v_readlane_b32 s10, v31, 48
	v_readlane_b32 s8, v31, 32
	v_readlane_b32 s6, v31, 16
	v_mov_b32_e32 v32, s10
	v_mul_f32_e32 v33, s8, v32
	v_cndmask_b32_e32 v32, 1.0, v32, vcc
	v_readlane_b32 s11, v30, 48
	v_mul_f32_e32 v34, s6, v33
	v_cndmask_b32_e64 v32, v32, v33, s[2:3]
	v_readlane_b32 s7, v30, 16
	v_cndmask_b32_e64 v32, v32, v34, s[4:5]
	v_mov_b32_e32 v33, s9
	v_mov_b32_e32 v34, s11
	v_fmac_f32_e32 v33, s8, v34
	v_mov_b32_e32 v35, s7
	v_cndmask_b32_e32 v34, 0, v34, vcc
	v_fmac_f32_e32 v35, s6, v33
	v_cndmask_b32_e64 v33, v34, v33, s[2:3]
	v_cndmask_b32_e64 v33, v33, v35, s[4:5]
	v_fmac_f32_e32 v30, v31, v33
	v_mul_f32_e32 v31, v31, v32
	v_readlane_b32 s6, v28, 0
	v_readlane_b32 s7, v24, 0
	v_readlane_b32 s4, v31, 0
	v_readlane_b32 s5, v30, 0
	v_cmp_eq_u32_e32 vcc, 0, v64
	s_and_saveexec_b64 s[2:3], vcc
	s_cbranch_execz .LBB0_4
	v_mov_b32_e32 v32, s4
	v_mov_b32_e32 v33, s7
	v_mov_b32_e32 v34, s5
	v_mul_f32_e32 v32, s6, v32
	v_lshlrev_b32_e32 v1, 2, v1
	v_fmac_f32_e32 v33, s6, v34
	ds_write2_b32 v1, v32, v33 offset1:4
